# P9: gather token loads for the next unit left in flight (wait deferred to last K-iteration)
# speedup vs baseline: 1.0023x; 1.0023x over previous
;     ...
;         const bool has_next = S.next(ui + 1, nxt);
;         const char* nA = has_next ? nxt.a : cA; const char* nB = has_next ? nxt.b : cB;
;         if constexpr (Sched::GATHER) { if (has_next) S.gather(nxt, voffA, gn); else {
; #pragma unroll
;             for (int h = 0; h < 2; ++h)
; #pragma unroll
;                 for (int i = 0; i < 2; ++i) gn[h][i] = gc[h][i]; } }
;     __device__ __forceinline__ void gather(const Unit& u, const unsigned (&voffA)[2], unsigned (&g)[2][2]) const {
;         const int ce = cnt[u.e];
; #pragma unroll
;         for (int i = 0; i < 2; ++i) { int R, C; stage_rc((int)threadIdx.x * 16 + i * 8192, R, C);
; #pragma unroll
;             for (int h = 0; h < 2; ++h) { const int pos = u.tl * 256 + h * 128 + R; const int pc = pos < ce ? pos : ce - 1; const int tok = list[2 * ((size_t)u.e * NTOK + pc)]; g[h][i] = (unsigned)tok * 2048u + voffA[i]; } }
.LBB5_1598:
	v_cndmask_b32_e64 v2, 0, 1, s[36:37]
	v_cmp_ne_u32_e64 s[0:1], 1, v2
	s_andn2_b64 vcc, exec, s[36:37]
	v_lshrrev_b32_e32 v218, 11, v206
	v_lshrrev_b32_e32 v201, 11, v204
	v_lshrrev_b32_e32 v220, 11, v207
	v_lshrrev_b32_e32 v219, 11, v205
	s_cbranch_vccnz .LBB5_1600
	s_lshl_b32 s19, s18, 2
	s_add_i32 s19, s19, 0
	s_add_i32 s19, s19, 0x20300
	v_mov_b32_e32 v2, s19
	ds_read_b32 v2, v2
	s_lshl_b32 s66, s58, 8
	s_ashr_i32 s19, s18, 31
	v_or_b32_e32 v4, s66, v1
	s_lshl_b64 s[40:41], s[18:19], 18
	s_waitcnt lgkmcnt(0)
	v_add_u32_e32 v8, -1, v2
	v_min_i32_e32 v2, v4, v8
	v_or_b32_e32 v4, 0x80, v4
	s_add_u32 s40, s15, s40
	v_min_i32_e32 v4, v4, v8
	v_or_b32_e32 v6, s66, v199
	v_or_b32_e32 v9, s66, v202
	v_ashrrev_i32_e32 v3, 31, v2
	s_addc_u32 s41, s27, s41
	v_ashrrev_i32_e32 v5, 31, v4
	v_min_i32_e32 v6, v6, v8
	v_min_i32_e32 v8, v9, v8
	v_lshl_add_u64 v[2:3], v[2:3], 3, s[40:41]
	v_lshl_add_u64 v[4:5], v[4:5], 3, s[40:41]
	v_ashrrev_i32_e32 v7, 31, v6
	v_ashrrev_i32_e32 v9, 31, v8
	v_lshl_add_u64 v[6:7], v[6:7], 3, s[40:41]
	v_lshl_add_u64 v[8:9], v[8:9], 3, s[40:41]
	global_load_dword v219, v[2:3], off
	s_nop 0
	global_load_dword v201, v[4:5], off
	s_nop 0
	global_load_dword v220, v[6:7], off
	global_load_dword v218, v[8:9], off

; #define PG8_STAGE_A(bufoff, gbase, h, go) do { if constexpr (Sched::GATHER) { PG8_STAGE(bufoff, gbase, go[h]); } else { PG8_STAGE(bufoff, (gbase) + (h) * hstep, voffA); } } while (0)
; #define PG8_LDA(dst, b, h) do { _Pragma("unroll") for (int m = 0; m < 4; ++m) _Pragma("unroll") for (int k = 0; k < 2; ++k) dst[m][k] = *(const LAS bf16x8*)(lds + PG8_SA(b, h) + aoff + m * 2048 + k * 1024); } while (0)
; #define PG8_LDB(dst, b, h) do { _Pragma("unroll") for (int n = 0; n < 2; ++n) _Pragma("unroll") for (int k = 0; k < 2; ++k) dst[n][k] = *(const LAS bf16x8*)(lds + PG8_SB(b, h) + boff + n * 2048 + k * 1024); } while (0)
; #define PG8_SCHED __builtin_amdgcn_sched_barrier(0)
;     ...
;             PG8_LDB(B0, 0, 0); PG8_LDB(B1, 0, 1); PG8_SCHED; PG8_LDA(At, 0, 0); PG8_STAGE_A(PG8_SA(1, 1), a1, 1, gc);
;             if constexpr (Sched::GATHER) { if (last) {
; #pragma unroll
;                 for (int h = 0; h < 2; ++h)
; #pragma unroll
;                     for (int i = 0; i < 2; ++i) gc[h][i] = gn[h][i]; } }
.LBB5_1602:
	ds_read_b128 v[18:21], v213
	ds_read_b128 v[26:29], v213 offset:2048
	v_xor_b32_e32 v213, 64, v213
	ds_read_b128 v[22:25], v213
	ds_read_b128 v[30:33], v213 offset:2048
	v_xor_b32_e32 v213, 64, v213
	ds_read_b128 v[2:5], v214
	ds_read_b128 v[10:13], v214 offset:2048
	v_xor_b32_e32 v214, 64, v214
	ds_read_b128 v[6:9], v214
	ds_read_b128 v[14:17], v214 offset:2048
	v_xor_b32_e32 v214, 64, v214
	s_cmp_eq_u32 s71, 12
	s_cselect_b64 s[38:39], -1, 0
	s_add_i32 m0, s44, 0xc000
	s_add_i32 s40, s44, 0xe000
	s_cmp_lg_u32 s71, 12
	v_mov_b32_e32 v194, v204
	ds_read_b128 v[58:61], v215
	ds_read_b128 v[50:53], v215 offset:2048
	ds_read_b128 v[42:45], v215 offset:4096
	ds_read_b128 v[34:37], v215 offset:6144
	v_xor_b32_e32 v215, 64, v215
	ds_read_b128 v[62:65], v215
	ds_read_b128 v[54:57], v215 offset:2048
	ds_read_b128 v[46:49], v215 offset:4096
	ds_read_b128 v[38:41], v215 offset:6144
	s_nop 0
	global_load_lds_dwordx4 v194, s[36:37]
	v_mov_b32_e32 v194, v206
	s_mov_b32 m0, s40
	s_nop 0
	global_load_lds_dwordx4 v194, s[36:37]
	s_cbranch_scc1 .LBB5_1601
	v_lshl_or_b32 v206, v218, 11, v203
	v_lshl_or_b32 v204, v201, 11, v203
	v_lshl_or_b32 v207, v220, 11, v203
	v_lshl_or_b32 v205, v219, 11, v203
	s_branch .LBB5_1601

; #define PG8_STAGE(bufoff, gbase, voff) do { _Pragma("unroll") for (int _i = 0; _i < 2; ++_i) { unsigned _vo = (voff)[_i]; asm volatile("" : "+v"(_vo)); \
;         __builtin_amdgcn_global_load_lds((const unsigned*)((const char*)(gbase) + _vo), (LAS unsigned*)(lds + (bufoff) + ldsw + _i * 8192), 16, 0, 0); } } while (0)
; #define PG8_STAGE_A(bufoff, gbase, h, go) do { if constexpr (Sched::GATHER) { PG8_STAGE(bufoff, gbase, go[h]); } else { PG8_STAGE(bufoff, (gbase) + (h) * hstep, voffA); } } while (0)
; #define PG8_LDA(dst, b, h) do { _Pragma("unroll") for (int m = 0; m < 4; ++m) _Pragma("unroll") for (int k = 0; k < 2; ++k) dst[m][k] = *(const LAS bf16x8*)(lds + PG8_SA(b, h) + aoff + m * 2048 + k * 1024); } while (0)
; #define PG8_LDB(dst, b, h) do { _Pragma("unroll") for (int n = 0; n < 2; ++n) _Pragma("unroll") for (int k = 0; k < 2; ++k) dst[n][k] = *(const LAS bf16x8*)(lds + PG8_SB(b, h) + boff + n * 2048 + k * 1024); } while (0)
; #define PG8_WAIT_V(n) asm volatile("s_waitcnt vmcnt(" #n ")" ::: "memory")
; #define PG8_WAIT_L(n) asm volatile("s_waitcnt lgkmcnt(" #n ")" ::: "memory")
; #define PG8_BAR __builtin_amdgcn_s_barrier()
; #define PG8_SCHED __builtin_amdgcn_sched_barrier(0)
;     ...
;             PG8_LDB(B0, 0, 0); PG8_LDB(B1, 0, 1); PG8_SCHED; PG8_LDA(At, 0, 0); PG8_STAGE_A(PG8_SA(1, 1), a1, 1, gc);
;             if constexpr (Sched::GATHER) { if (last) {
; #pragma unroll
;                 for (int h = 0; h < 2; ++h)
; #pragma unroll
;                     for (int i = 0; i < 2; ++i) gc[h][i] = gn[h][i]; } }
;             PG8_WAIT_V(8); PG8_WAIT_L(0); PG8_BAR; PG8_MMA(0, 0, At, B0); PG8_MMA(0, 1, At, B1); PG8_BAR; PG8_SCHED;
;             PG8_LDA(At, 0, 1); PG8_STAGE(PG8_SB(0, 0), b2, voffB); PG8_STAGE(PG8_SB(0, 1), b2 + hstep, voffB); PG8_STAGE_A(PG8_SA(0, 0), a2, 0, gc);
;             PG8_WAIT_V(8); PG8_WAIT_L(0); PG8_BAR; PG8_MMA(1, 0, At, B0); PG8_MMA(1, 1, At, B1); PG8_BAR; PG8_SCHED;
.LBB5_1678:
	ds_read_b128 v[130:133], v146
	ds_read_b128 v[152:155], v146 offset:2048
	v_xor_b32_e32 v146, 64, v146
	ds_read_b128 v[134:137], v146
	ds_read_b128 v[156:159], v146 offset:2048
	v_xor_b32_e32 v146, 64, v146
	ds_read_b128 v[160:163], v147
	ds_read_b128 v[168:171], v147 offset:2048
	v_xor_b32_e32 v147, 64, v147
	ds_read_b128 v[164:167], v147
	ds_read_b128 v[172:175], v147 offset:2048
	v_xor_b32_e32 v147, 64, v147
	s_add_u32 s34, s18, 0xfffc0080
	s_addc_u32 s35, s19, -1
	s_cmp_eq_u32 s64, 12
	s_cselect_b32 s35, s58, s35
	s_cselect_b32 s34, s59, s34
	s_cselect_b32 s37, s60, s63
	s_cselect_b32 s36, s61, s62
	v_mov_b32_e32 v138, v1
	ds_read_b128 v[176:179], v148
	ds_read_b128 v[184:187], v148 offset:2048
	ds_read_b128 v[200:203], v148 offset:4096
	ds_read_b128 v[208:211], v148 offset:6144
	v_xor_b32_e32 v148, 64, v148
	ds_read_b128 v[180:183], v148
	ds_read_b128 v[188:191], v148 offset:2048
	ds_read_b128 v[204:207], v148 offset:4096
	ds_read_b128 v[212:215], v148 offset:6144
	s_add_u32 s98, s62, 0x3ff80
	s_addc_u32 s99, s63, 0
	s_add_i32 s100, s40, 0x1c000
	v_mov_b32_e32 v138, v140
	s_mov_b32 m0, s100
	s_nop 0
	global_load_lds_dwordx4 v138, s[98:99]
	v_mov_b32_e32 v138, v142
	s_add_i32 m0, s100, 0x2000
	s_nop 0
	global_load_lds_dwordx4 v138, s[98:99]
	v_mov_b32_e32 v138, v1
	s_add_i32 m0, s41, 0xc000
	s_nop 0
	global_load_lds_dwordx4 v138, s[18:19]
	v_mov_b32_e32 v138, v141
	s_add_i32 m0, s41, 0xe000
	s_nop 0
	global_load_lds_dwordx4 v138, s[18:19]
	s_waitcnt vmcnt(8)
	s_waitcnt lgkmcnt(0)
	s_barrier
	s_setprio 1
	s_waitcnt lgkmcnt(0)
	v_mfma_scale_f32_16x16x128_f8f6f4 v[126:129], v[130:137], v[176:183], v[126:129], v149, v149 op_sel_hi:[0,0,0]
	v_mfma_scale_f32_16x16x128_f8f6f4 v[122:125], v[152:159], v[176:183], v[122:125], v149, v149 op_sel_hi:[0,0,0]
	v_mfma_scale_f32_16x16x128_f8f6f4 v[118:121], v[130:137], v[184:191], v[118:121], v149, v149 op_sel_hi:[0,0,0]
	v_mfma_scale_f32_16x16x128_f8f6f4 v[114:117], v[152:159], v[184:191], v[114:117], v149, v149 op_sel_hi:[0,0,0]
	v_mfma_scale_f32_16x16x128_f8f6f4 v[110:113], v[130:137], v[200:207], v[110:113], v149, v149 op_sel_hi:[0,0,0]
	v_mfma_scale_f32_16x16x128_f8f6f4 v[106:109], v[152:159], v[200:207], v[106:109], v149, v149 op_sel_hi:[0,0,0]
	v_mfma_scale_f32_16x16x128_f8f6f4 v[102:105], v[130:137], v[208:215], v[102:105], v149, v149 op_sel_hi:[0,0,0]
	v_mfma_scale_f32_16x16x128_f8f6f4 v[98:101], v[152:159], v[208:215], v[98:101], v149, v149 op_sel_hi:[0,0,0]
	s_setprio 0
	s_setprio 1
	v_mfma_scale_f32_16x16x128_f8f6f4 v[192:195], v[160:167], v[176:183], v[70:73], v149, v149 op_sel_hi:[0,0,0]
	v_mfma_scale_f32_16x16x128_f8f6f4 v[176:179], v[168:175], v[176:183], v[66:69], v149, v149 op_sel_hi:[0,0,0]
	v_mfma_scale_f32_16x16x128_f8f6f4 v[180:183], v[160:167], v[184:191], v[54:57], v149, v149 op_sel_hi:[0,0,0]
	v_mfma_scale_f32_16x16x128_f8f6f4 v[184:187], v[168:175], v[184:191], v[50:53], v149, v149 op_sel_hi:[0,0,0]
	v_mfma_scale_f32_16x16x128_f8f6f4 v[188:191], v[160:167], v[200:207], v[46:49], v149, v149 op_sel_hi:[0,0,0]
	v_mfma_scale_f32_16x16x128_f8f6f4 v[200:203], v[168:175], v[200:207], v[42:45], v149, v149 op_sel_hi:[0,0,0]
	v_mfma_scale_f32_16x16x128_f8f6f4 v[204:207], v[160:167], v[208:215], v[38:41], v149, v149 op_sel_hi:[0,0,0]
	v_mfma_scale_f32_16x16x128_f8f6f4 v[208:211], v[168:175], v[208:215], v[34:37], v149, v149 op_sel_hi:[0,0,0]
	s_setprio 0
	s_barrier
	v_mov_b32_e32 v138, v140
	s_add_i32 s65, s50, s40
	s_nop 2
	ds_read_b128 v[38:41], v148 offset:16384
	ds_read_b128 v[46:49], v148 offset:18432
	ds_read_b128 v[54:57], v148 offset:20480
	ds_read_b128 v[70:73], v148 offset:22528
	v_xor_b32_e32 v148, 64, v148
	ds_read_b128 v[34:37], v148 offset:16384
	ds_read_b128 v[42:45], v148 offset:18432
	ds_read_b128 v[50:53], v148 offset:20480
	ds_read_b128 v[66:69], v148 offset:22528
	s_mov_b32 m0, s65
	s_nop 0
	global_load_lds_dwordx4 v138, s[36:37]
	v_mov_b32_e32 v138, v142
	s_add_i32 m0, s65, 0x2000
	s_nop 0
	global_load_lds_dwordx4 v138, s[36:37]
	v_mov_b32_e32 v138, v1
	s_mov_b32 m0, s41
	s_nop 0
	global_load_lds_dwordx4 v138, s[34:35]
	v_mov_b32_e32 v138, v141
	s_mov_b32 m0, s42
	s_nop 0
	global_load_lds_dwordx4 v138, s[34:35]
	s_waitcnt vmcnt(6)
	s_waitcnt lgkmcnt(0)
	s_barrier
	s_setprio 1
	s_waitcnt lgkmcnt(0)
	v_mfma_scale_f32_16x16x128_f8f6f4 v[94:97], v[130:137], v[34:41], v[94:97], v149, v149 op_sel_hi:[0,0,0]
	v_mfma_scale_f32_16x16x128_f8f6f4 v[90:93], v[152:159], v[34:41], v[90:93], v149, v149 op_sel_hi:[0,0,0]
	v_mfma_scale_f32_16x16x128_f8f6f4 v[86:89], v[130:137], v[42:49], v[86:89], v149, v149 op_sel_hi:[0,0,0]
	v_mfma_scale_f32_16x16x128_f8f6f4 v[82:85], v[152:159], v[42:49], v[82:85], v149, v149 op_sel_hi:[0,0,0]
	v_mfma_scale_f32_16x16x128_f8f6f4 v[78:81], v[130:137], v[50:57], v[78:81], v149, v149 op_sel_hi:[0,0,0]
	v_mfma_scale_f32_16x16x128_f8f6f4 v[74:77], v[152:159], v[50:57], v[74:77], v149, v149 op_sel_hi:[0,0,0]
	v_mfma_scale_f32_16x16x128_f8f6f4 v[212:215], v[130:137], v[66:73], v[62:65], v149, v149 op_sel_hi:[0,0,0]
	v_mfma_scale_f32_16x16x128_f8f6f4 v[216:219], v[152:159], v[66:73], v[58:61], v149, v149 op_sel_hi:[0,0,0]
	s_setprio 0
	s_setprio 1
	v_mfma_scale_f32_16x16x128_f8f6f4 v[220:223], v[160:167], v[34:41], v[30:33], v149, v149 op_sel_hi:[0,0,0]
	v_mfma_scale_f32_16x16x128_f8f6f4 v[224:227], v[168:175], v[34:41], v[26:29], v149, v149 op_sel_hi:[0,0,0]
	v_mfma_scale_f32_16x16x128_f8f6f4 v[228:231], v[160:167], v[42:49], v[22:25], v149, v149 op_sel_hi:[0,0,0]
	v_mfma_scale_f32_16x16x128_f8f6f4 v[232:235], v[168:175], v[42:49], v[18:21], v149, v149 op_sel_hi:[0,0,0]
	v_mfma_scale_f32_16x16x128_f8f6f4 v[236:239], v[160:167], v[50:57], v[14:17], v149, v149 op_sel_hi:[0,0,0]
	v_mfma_scale_f32_16x16x128_f8f6f4 v[240:243], v[168:175], v[50:57], v[10:13], v149, v149 op_sel_hi:[0,0,0]
	v_mfma_scale_f32_16x16x128_f8f6f4 v[244:247], v[160:167], v[66:73], v[6:9], v149, v149 op_sel_hi:[0,0,0]
	v_mfma_scale_f32_16x16x128_f8f6f4 v[248:251], v[168:175], v[66:73], v[2:5], v149, v149 op_sel_hi:[0,0,0]
	s_setprio 0
	s_barrier
; #define PG8_STAGE(bufoff, gbase, voff) do { _Pragma("unroll") for (int _i = 0; _i < 2; ++_i) { unsigned _vo = (voff)[_i]; asm volatile("" : "+v"(_vo)); \
;         __builtin_amdgcn_global_load_lds((const unsigned*)((const char*)(gbase) + _vo), (LAS unsigned*)(lds + (bufoff) + ldsw + _i * 8192), 16, 0, 0); } } while (0)
; #define PG8_STAGE_A(bufoff, gbase, h, go) do { if constexpr (Sched::GATHER) { PG8_STAGE(bufoff, gbase, go[h]); } else { PG8_STAGE(bufoff, (gbase) + (h) * hstep, voffA); } } while (0)
; #define PG8_LDA(dst, b, h) do { _Pragma("unroll") for (int m = 0; m < 4; ++m) _Pragma("unroll") for (int k = 0; k < 2; ++k) dst[m][k] = *(const LAS bf16x8*)(lds + PG8_SA(b, h) + aoff + m * 2048 + k * 1024); } while (0)
; #define PG8_LDB(dst, b, h) do { _Pragma("unroll") for (int n = 0; n < 2; ++n) _Pragma("unroll") for (int k = 0; k < 2; ++k) dst[n][k] = *(const LAS bf16x8*)(lds + PG8_SB(b, h) + boff + n * 2048 + k * 1024); } while (0)
; #define PG8_WAIT_V(n) asm volatile("s_waitcnt vmcnt(" #n ")" ::: "memory")
; #define PG8_WAIT_L(n) asm volatile("s_waitcnt lgkmcnt(" #n ")" ::: "memory")
; #define PG8_BAR __builtin_amdgcn_s_barrier()
; #define PG8_SCHED __builtin_amdgcn_sched_barrier(0)
;     ...
;             PG8_LDB(B0, 1, 0); PG8_LDB(B1, 1, 1); PG8_SCHED; PG8_LDA(At, 1, 0); PG8_STAGE_A(PG8_SA(0, 1), a2, 1, gc);
;             PG8_WAIT_V(8); PG8_WAIT_L(0); PG8_BAR; PG8_MMA(0, 0, At, B0); PG8_MMA(0, 1, At, B1); PG8_BAR; PG8_SCHED;
;             PG8_LDA(At, 1, 1); PG8_STAGE(PG8_SB(1, 0), b3, voffB); PG8_STAGE(PG8_SB(1, 1), b3 + hstep, voffB); PG8_STAGE_A(PG8_SA(1, 0), a3, 0, gc);
;             PG8_WAIT_V(8); PG8_WAIT_L(0); PG8_BAR; PG8_MMA(1, 0, At, B0); PG8_MMA(1, 1, At, B1); PG8_BAR; PG8_SCHED;
;         }
	s_add_i32 s65, 0, 0x18000
	s_add_i32 s68, 0, 0x1c000
	v_add_u32_e32 v14, s65, v145
	v_add_u32_e32 v18, s68, v145
	s_nop 0
	ds_read_b128 v[2:5], v14
	ds_read_b128 v[10:13], v14 offset:2048
	v_xor_b32_e32 v14, 64, v14
	ds_read_b128 v[6:9], v14
	ds_read_b128 v[14:17], v14 offset:2048
	ds_read_b128 v[130:133], v18
	ds_read_b128 v[152:155], v18 offset:2048
	v_xor_b32_e32 v18, 64, v18
	ds_read_b128 v[134:137], v18
	ds_read_b128 v[156:159], v18 offset:2048
	s_add_u32 s66, s34, 0x40000
	v_mov_b32_e32 v42, v1
	s_mov_b32 m0, s43
	ds_read_b128 v[18:21], v148 offset:32768
	ds_read_b128 v[26:29], v148 offset:34816
	ds_read_b128 v[34:37], v148 offset:36864
	ds_read_b128 v[58:61], v148 offset:38912
	v_xor_b32_e32 v148, 64, v148
	ds_read_b128 v[22:25], v148 offset:32768
	ds_read_b128 v[30:33], v148 offset:34816
	ds_read_b128 v[38:41], v148 offset:36864
	ds_read_b128 v[62:65], v148 offset:38912
	s_addc_u32 s67, s35, 0
	s_add_u32 s98, s36, 0x40000
	s_addc_u32 s99, s37, 0
	s_add_i32 s100, s51, s40
	v_mov_b32_e32 v42, v140
	s_mov_b32 m0, s100
	s_nop 0
	global_load_lds_dwordx4 v42, s[98:99]
	v_mov_b32_e32 v42, v142
	s_add_i32 m0, s100, 0x2000
	s_nop 0
	global_load_lds_dwordx4 v42, s[98:99]
	v_mov_b32_e32 v42, v1
	s_mov_b32 m0, s43
	s_nop 0
	global_load_lds_dwordx4 v42, s[66:67]
	v_mov_b32_e32 v42, v141
	s_mov_b32 m0, s44
	s_nop 0
	global_load_lds_dwordx4 v42, s[66:67]
	s_waitcnt vmcnt(8)
	s_waitcnt lgkmcnt(0)
	s_barrier
	s_setprio 1
	s_waitcnt lgkmcnt(0)
	v_mfma_scale_f32_16x16x128_f8f6f4 v[126:129], v[2:9], v[18:25], v[126:129], v149, v149 op_sel_hi:[0,0,0]
	v_mfma_scale_f32_16x16x128_f8f6f4 v[122:125], v[10:17], v[18:25], v[122:125], v149, v149 op_sel_hi:[0,0,0]
	v_mfma_scale_f32_16x16x128_f8f6f4 v[118:121], v[2:9], v[26:33], v[118:121], v149, v149 op_sel_hi:[0,0,0]
	v_mfma_scale_f32_16x16x128_f8f6f4 v[114:117], v[10:17], v[26:33], v[114:117], v149, v149 op_sel_hi:[0,0,0]
	v_mfma_scale_f32_16x16x128_f8f6f4 v[110:113], v[2:9], v[34:41], v[110:113], v149, v149 op_sel_hi:[0,0,0]
	v_mfma_scale_f32_16x16x128_f8f6f4 v[106:109], v[10:17], v[34:41], v[106:109], v149, v149 op_sel_hi:[0,0,0]
	v_mfma_scale_f32_16x16x128_f8f6f4 v[102:105], v[2:9], v[58:65], v[102:105], v149, v149 op_sel_hi:[0,0,0]
	v_mfma_scale_f32_16x16x128_f8f6f4 v[98:101], v[10:17], v[58:65], v[98:101], v149, v149 op_sel_hi:[0,0,0]
	s_setprio 0
	s_setprio 1
	v_mfma_scale_f32_16x16x128_f8f6f4 v[70:73], v[130:137], v[18:25], v[192:195], v149, v149 op_sel_hi:[0,0,0]
	v_mfma_scale_f32_16x16x128_f8f6f4 v[66:69], v[152:159], v[18:25], v[176:179], v149, v149 op_sel_hi:[0,0,0]
	v_mfma_scale_f32_16x16x128_f8f6f4 v[54:57], v[130:137], v[26:33], v[180:183], v149, v149 op_sel_hi:[0,0,0]
	v_mfma_scale_f32_16x16x128_f8f6f4 v[50:53], v[152:159], v[26:33], v[184:187], v149, v149 op_sel_hi:[0,0,0]
	v_mfma_scale_f32_16x16x128_f8f6f4 v[46:49], v[130:137], v[34:41], v[188:191], v149, v149 op_sel_hi:[0,0,0]
	v_mfma_scale_f32_16x16x128_f8f6f4 v[42:45], v[152:159], v[34:41], v[200:203], v149, v149 op_sel_hi:[0,0,0]
	v_mfma_scale_f32_16x16x128_f8f6f4 v[38:41], v[130:137], v[58:65], v[204:207], v149, v149 op_sel_hi:[0,0,0]
	v_mfma_scale_f32_16x16x128_f8f6f4 v[34:37], v[152:159], v[58:65], v[208:211], v149, v149 op_sel_hi:[0,0,0]
	s_setprio 0
	s_barrier
	v_mov_b32_e32 v138, v140
	ds_read_b128 v[22:25], v148 offset:49152
	ds_read_b128 v[164:167], v148 offset:51200
	ds_read_b128 v[172:175], v148 offset:53248
	ds_read_b128 v[180:183], v148 offset:55296
	v_xor_b32_e32 v148, 64, v148
	ds_read_b128 v[18:21], v148 offset:49152
	ds_read_b128 v[160:163], v148 offset:51200
	ds_read_b128 v[168:171], v148 offset:53248
	ds_read_b128 v[176:179], v148 offset:55296
	s_add_i32 s65, s65, s40
	v_lshl_add_u64 v[26:27], s[36:37], 0, v[138:139]
	v_lshl_add_u64 v[26:27], v[26:27], 0, s[6:7]
	s_mov_b32 m0, s65
	v_mov_b32_e32 v138, v142
	global_load_lds_dwordx4 v[26:27], off
	s_add_i32 m0, s65, 0x2000
	v_lshl_add_u64 v[26:27], s[36:37], 0, v[138:139]
	v_lshl_add_u64 v[26:27], v[26:27], 0, s[6:7]
	s_add_u32 s36, s36, 0x40080
	global_load_lds_dwordx4 v[26:27], off
	s_addc_u32 s37, s37, 0
	v_mov_b32_e32 v138, v1
	s_mov_b32 m0, s47
	v_lshl_add_u64 v[26:27], s[34:35], 0, v[138:139]
	v_lshl_add_u64 v[26:27], v[26:27], 0, s[6:7]
	v_mov_b32_e32 v138, v141
	global_load_lds_dwordx4 v[26:27], off
	s_mov_b32 m0, s48
	v_lshl_add_u64 v[26:27], s[34:35], 0, v[138:139]
	v_lshl_add_u64 v[26:27], v[26:27], 0, s[6:7]
	global_load_lds_dwordx4 v[26:27], off
	s_waitcnt vmcnt(6)
	s_waitcnt lgkmcnt(0)
	s_barrier
	s_setprio 1
	s_waitcnt lgkmcnt(0)
	v_mfma_scale_f32_16x16x128_f8f6f4 v[94:97], v[2:9], v[18:25], v[94:97], v149, v149 op_sel_hi:[0,0,0]
	v_mfma_scale_f32_16x16x128_f8f6f4 v[90:93], v[10:17], v[18:25], v[90:93], v149, v149 op_sel_hi:[0,0,0]
	v_mfma_scale_f32_16x16x128_f8f6f4 v[86:89], v[2:9], v[160:167], v[86:89], v149, v149 op_sel_hi:[0,0,0]
	v_mfma_scale_f32_16x16x128_f8f6f4 v[82:85], v[10:17], v[160:167], v[82:85], v149, v149 op_sel_hi:[0,0,0]
	v_mfma_scale_f32_16x16x128_f8f6f4 v[78:81], v[2:9], v[168:175], v[78:81], v149, v149 op_sel_hi:[0,0,0]
	v_mfma_scale_f32_16x16x128_f8f6f4 v[74:77], v[10:17], v[168:175], v[74:77], v149, v149 op_sel_hi:[0,0,0]
	v_mfma_scale_f32_16x16x128_f8f6f4 v[62:65], v[2:9], v[176:183], v[212:215], v149, v149 op_sel_hi:[0,0,0]
	v_mfma_scale_f32_16x16x128_f8f6f4 v[58:61], v[10:17], v[176:183], v[216:219], v149, v149 op_sel_hi:[0,0,0]
	s_setprio 0
	s_setprio 1
	v_mfma_scale_f32_16x16x128_f8f6f4 v[30:33], v[130:137], v[18:25], v[220:223], v149, v149 op_sel_hi:[0,0,0]
	v_mfma_scale_f32_16x16x128_f8f6f4 v[26:29], v[152:159], v[18:25], v[224:227], v149, v149 op_sel_hi:[0,0,0]
	v_mfma_scale_f32_16x16x128_f8f6f4 v[22:25], v[130:137], v[160:167], v[228:231], v149, v149 op_sel_hi:[0,0,0]
	v_mfma_scale_f32_16x16x128_f8f6f4 v[18:21], v[152:159], v[160:167], v[232:235], v149, v149 op_sel_hi:[0,0,0]
	v_mfma_scale_f32_16x16x128_f8f6f4 v[14:17], v[130:137], v[168:175], v[236:239], v149, v149 op_sel_hi:[0,0,0]
	v_mfma_scale_f32_16x16x128_f8f6f4 v[10:13], v[152:159], v[168:175], v[240:243], v149, v149 op_sel_hi:[0,0,0]
	v_mfma_scale_f32_16x16x128_f8f6f4 v[6:9], v[130:137], v[176:183], v[244:247], v149, v149 op_sel_hi:[0,0,0]
	v_mfma_scale_f32_16x16x128_f8f6f4 v[2:5], v[152:159], v[176:183], v[248:251], v149, v149 op_sel_hi:[0,0,0]
	s_setprio 0
	s_barrier
	s_add_i32 s64, s64, 2
	s_add_u32 s18, s18, 0x100
	s_addc_u32 s19, s19, 0
	s_add_u32 s62, s62, 0x100
	s_addc_u32 s63, s63, 0
	s_cmp_gt_u32 s64, 13
	s_cbranch_scc0 .LBB5_1678
	s_and_b64 vcc, exec, s[8:9]
	s_cbranch_vccz .LBB5_1681
	s_barrier

; #define LAS __attribute__((address_space(3)))
; __global__ void __launch_bounds__(NWAVES * 64, 2) fwd(P p) {
;     extern __shared__ __attribute__((aligned(16))) unsigned char lds_raw[];
;     LAS unsigned char* lds = (LAS unsigned char*)lds_raw;
;     volatile LAS unsigned* MISC = (volatile LAS unsigned*)(lds + MISC_OFF);
;     const int tid = threadIdx.x, lane = tid & 63, wave = __builtin_amdgcn_readfirstlane(tid >> 6);
	.amdhsa_kernel _Z3fwd1P
		.amdhsa_group_segment_fixed_size 0
		.amdhsa_private_segment_fixed_size 0
		.amdhsa_kernarg_size 512
		.amdhsa_user_sgpr_count 2
		.amdhsa_user_sgpr_dispatch_ptr 0
		.amdhsa_user_sgpr_queue_ptr 0
		.amdhsa_user_sgpr_kernarg_segment_ptr 1
		.amdhsa_user_sgpr_dispatch_id 0
		.amdhsa_user_sgpr_kernarg_preload_length 0
		.amdhsa_user_sgpr_kernarg_preload_offset 0
		.amdhsa_user_sgpr_private_segment_size 0
		.amdhsa_uses_dynamic_stack 0
		.amdhsa_enable_private_segment 0
		.amdhsa_system_sgpr_workgroup_id_x 1
		.amdhsa_system_sgpr_workgroup_id_y 0
		.amdhsa_system_sgpr_workgroup_id_z 0
		.amdhsa_system_sgpr_workgroup_info 0
		.amdhsa_system_vgpr_workitem_id 0
		.amdhsa_next_free_vgpr 254
		.amdhsa_next_free_sgpr 101
		.amdhsa_accum_offset 256
		.amdhsa_reserve_vcc 1
		.amdhsa_float_round_mode_32 0
		.amdhsa_float_round_mode_16_64 0
		.amdhsa_float_denorm_mode_32 3
		.amdhsa_float_denorm_mode_16_64 3
		.amdhsa_dx10_clamp 1
		.amdhsa_ieee_mode 1
		.amdhsa_fp16_overflow 0
		.amdhsa_tg_split 0
		.amdhsa_exception_fp_ieee_invalid_op 0
		.amdhsa_exception_fp_denorm_src 0
		.amdhsa_exception_fp_ieee_div_zero 0
		.amdhsa_exception_fp_ieee_overflow 0
		.amdhsa_exception_fp_ieee_underflow 0
		.amdhsa_exception_fp_ieee_inexact 0
		.amdhsa_exception_int_div_zero 0
	.end_amdhsa_kernel

; __global__ void __launch_bounds__(256) n_attn(const bf16* __restrict__ qkxy, const bf16* __restrict__ vt, const float* __restrict__ rel, bf16* mix, float* ssa) {
;     const int blk = blockIdx.x, tq = (blk & 7) * 256 + threadIdx.x, bh = blk >> 3, h = bh & 15, b = bh >> 4;
;     const size_t m = (size_t)b * SEQ + tq;
;     const bf16* Q = qkxy; const bf16* Kp = qkxy + (size_t)NTOK * 1024;
;     float q[64], o[64];
; #pragma unroll
;     for (int d = 0; d < 64; ++d) { q[d] = bf2f(Q[m * 1024 + h * 64 + d]); o[d] = 0.f; }
;     float mx = -INFINITY, l = 0.f;
;     const int c = tq >> 6, k0 = (c > LEFTC ? c - LEFTC : 0) * 64, k1 = (c + 1) * 64;
;     const float* tab = rel + h * RELW;
;     for (int key = k0; key < k1; ++key) {
;         const bf16* kr = Kp + ((size_t)b * SEQ + key) * 1024 + h * 64;
;         float s = 0.f;
; #pragma unroll
;         for (int d = 0; d < 64; ++d) s += q[d] * bf2f(kr[d]);
;         int r = tq - key; r = (r < -MAXREL ? -MAXREL : (r > MAXREL ? MAXREL : r)) + MAXREL;
;         s += tab[r] * LOG2E;
;         const float mn = fmaxf(mx, s), corr = exp2f(mx - mn), pe = exp2f(s - mn);
;         l = l * corr + pe;
;         const bf16* vp = vt + (size_t)(h * 64) * NTOK + (size_t)b * SEQ + key;
; #pragma unroll
;         for (int d = 0; d < 64; ++d) o[d] = o[d] * corr + pe * bf2f(vp[(size_t)d * NTOK]);
;         mx = mn;
;     }
;     const float il = 1.0f / l; float ss = 0.f;
; #pragma unroll
;     for (int d = 0; d < 64; ++d) { const float v = o[d] * il; ss += v * v; mix[m * DM + h * 64 + d] = (bf16)f2bf(v); }
;     ssa[m * 16 + h] = ss;
; }
; __global__ void __launch_bounds__(256) n_xattn(const bf16* __restrict__ cq, const bf16* __restrict__ ck, const bf16* __restrict__ cvt, bf16* ox) {
; __global__ void __launch_bounds__(256) n_lru_a(const bf16* __restrict__ xr, const float* __restrict__ conv_w, const float* __restrict__ conv_b, const bf16* __restrict__ wga_t, const float* __restrict__ b_ga, ...
;     const size_t idx = (size_t)blockIdx.x * 256 + threadIdx.x; const int c = (int)(idx & 1023); const size_t m = idx >> 10; const int t = (int)(m & (SEQ - 1)), n = c >> 7, d = c & 127;
;     float rp = b_ga[c], ip = b_gx[c], xown = 0.f;
;     const bf16* wa = wga_t + (size_t)(n * 128 + d) * 128; const bf16* wx = wgx_t + (size_t)(n * 128 + d) * 128;
;     for (int cp = 0; cp < 128; ++cp) { const int cc = n * 128 + cp; float xc = conv_b[cc];
amdhsa.kernels:
  - .agpr_count:     0
    .args:
      - .actual_access:  read_only
        .address_space:  global
        .offset:         0
        .size:           8
        .value_kind:     global_buffer
      - .actual_access:  read_only
        .address_space:  global
        .offset:         8
        .size:           8
        .value_kind:     global_buffer
      - .actual_access:  read_only
        .address_space:  global
        .offset:         16
        .size:           8
        .value_kind:     global_buffer
      - .address_space:  global
        .offset:         24
        .size:           8
        .value_kind:     global_buffer
      - .address_space:  global
        .offset:         32
        .size:           8
        .value_kind:     global_buffer
    .group_segment_fixed_size: 0
    .kernarg_segment_align: 8
    .kernarg_segment_size: 40
    .language:       OpenCL C
    .language_version:
      - 2
      - 0
    .max_flat_workgroup_size: 256
    .name:           _Z6n_attnPKtS0_PKfPtPf
    .private_segment_fixed_size: 0
    .sgpr_count:     82
    .sgpr_spill_count: 0
    .symbol:         _Z6n_attnPKtS0_PKfPtPf.kd
    .uniform_work_group_size: 1
    .uses_dynamic_stack: false
    .vgpr_count:     152
    .vgpr_spill_count: 0
    .wavefront_size: 64
  - .agpr_count:     0
    .args:
      - .actual_access:  read_only
        .address_space:  global
        .offset:         0
        .size:           8
        .value_kind:     global_buffer
      - .actual_access:  read_only
        .address_space:  global
        .offset:         8
        .size:           8
        .value_kind:     global_buffer
      - .actual_access:  read_only
        .address_space:  global
        .offset:         16
        .size:           8
        .value_kind:     global_buffer
      - .address_space:  global
        .offset:         24
        .size:           8
        .value_kind:     global_buffer
    .group_segment_fixed_size: 0
    .kernarg_segment_align: 8
    .kernarg_segment_size: 32
    .language:       OpenCL C
    .language_version:
      - 2
      - 0
    .max_flat_workgroup_size: 256
    .name:           _Z7n_xattnPKtS0_S0_Pt
    .private_segment_fixed_size: 0
    .sgpr_count:     24
    .sgpr_spill_count: 0
    .symbol:         _Z7n_xattnPKtS0_S0_Pt.kd
    .uniform_work_group_size: 1
    .uses_dynamic_stack: false
    .vgpr_count:     256
    .vgpr_spill_count: 0
    .wavefront_size: 64
  - .agpr_count:     0
    .args:
      - .actual_access:  read_only
        .address_space:  global
        .offset:         0
        .size:           8
        .value_kind:     global_buffer
      - .actual_access:  read_only
        .address_space:  global
        .offset:         8
        .size:           8
        .value_kind:     global_buffer
      - .actual_access:  read_only
        .address_space:  global
        .offset:         16
        .size:           8
        .value_kind:     global_buffer
      - .actual_access:  read_only
        .address_space:  global
        .offset:         24
        .size:           8
        .value_kind:     global_buffer
      - .actual_access:  read_only
        .address_space:  global
        .offset:         32
        .size:           8
        .value_kind:     global_buffer
      - .actual_access:  read_only
        .address_space:  global
        .offset:         40
        .size:           8
        .value_kind:     global_buffer
      - .actual_access:  read_only
        .address_space:  global
        .offset:         48
        .size:           8
        .value_kind:     global_buffer
      - .actual_access:  read_only
        .address_space:  global
        .offset:         56
        .size:           8
        .value_kind:     global_buffer
      - .address_space:  global
        .offset:         64
        .size:           8
        .value_kind:     global_buffer
      - .address_space:  global
        .offset:         72
        .size:           8
        .value_kind:     global_buffer
    .group_segment_fixed_size: 0
    .kernarg_segment_align: 8
    .kernarg_segment_size: 80
    .language:       OpenCL C
    .language_version:
      - 2
      - 0
    .max_flat_workgroup_size: 256
    .name:           _Z7n_lru_aPKtPKfS2_S0_S2_S0_S2_S2_PfS3_
    .private_segment_fixed_size: 0
    .sgpr_count:     30
    .sgpr_spill_count: 0
    .symbol:         _Z7n_lru_aPKtPKfS2_S0_S2_S0_S2_S2_PfS3_.kd
    .uniform_work_group_size: 1
    .uses_dynamic_stack: false
    .vgpr_count:     30
    .vgpr_spill_count: 0
    .wavefront_size: 64
  - .agpr_count:     0
    .args:
      - .actual_access:  read_only
        .address_space:  global
        .offset:         0
        .size:           8
        .value_kind:     global_buffer
      - .actual_access:  read_only
        .address_space:  global
        .offset:         8
        .size:           8
        .value_kind:     global_buffer
      - .actual_access:  read_only
        .address_space:  global
        .offset:         16
        .size:           8
        .value_kind:     global_buffer
      - .address_space:  global
        .offset:         24
        .size:           8
        .value_kind:     global_buffer
      - .address_space:  global
        .offset:         32
        .size:           8
        .value_kind:     global_buffer
    .group_segment_fixed_size: 0
    .kernarg_segment_align: 8
    .kernarg_segment_size: 40
    .language:       OpenCL C
    .language_version:
      - 2
      - 0
    .max_flat_workgroup_size: 64
    .name:           _Z7n_lru_bPKfS0_PKtPtPf
    .private_segment_fixed_size: 0
    .sgpr_count:     22
    .sgpr_spill_count: 0
    .symbol:         _Z7n_lru_bPKfS0_PKtPtPf.kd
    .uniform_work_group_size: 1
    .uses_dynamic_stack: false
    .vgpr_count:     26
    .vgpr_spill_count: 0
    .wavefront_size: 64
; #define LAS __attribute__((address_space(3)))
; __global__ void __launch_bounds__(NWAVES * 64, 2) fwd(P p) {
;     extern __shared__ __attribute__((aligned(16))) unsigned char lds_raw[];
;     LAS unsigned char* lds = (LAS unsigned char*)lds_raw;
;     volatile LAS unsigned* MISC = (volatile LAS unsigned*)(lds + MISC_OFF);
;     const int tid = threadIdx.x, lane = tid & 63, wave = __builtin_amdgcn_readfirstlane(tid >> 6);
;     const int G = gridDim.x, bx = blockIdx.x; const int vcu = (G % 8 == 0) ? (bx % 8) * (G / 8) + bx / 8 : bx;
;     const int gw = vcu * NWAVES + wave, NGW = G * NWAVES;
;     for (int u = tid; u < (LDS_BYTES - LDSCTL_OFF) / 4; u += NWAVES * 64) ((LAS unsigned*)(lds + LDSCTL_OFF))[u] = 0u;
;     __syncthreads();
  - .agpr_count:     0
    .args:
      - .address_space:  global
        .offset:         0
        .size:           8
        .value_kind:     global_buffer
      - .address_space:  global
        .offset:         8
        .size:           8
        .value_kind:     global_buffer
    .group_segment_fixed_size: 0
    .kernarg_segment_align: 8
    .kernarg_segment_size: 16
    .language:       OpenCL C
    .language_version:
      - 2
      - 0
    .max_flat_workgroup_size: 1024
    .name:           _Z6n_toffPKiPi
    .private_segment_fixed_size: 0
    .sgpr_count:     10
    .sgpr_spill_count: 0
    .symbol:         _Z6n_toffPKiPi.kd
    .uniform_work_group_size: 1
    .uses_dynamic_stack: false
    .vgpr_count:     3
    .vgpr_spill_count: 0
    .wavefront_size: 64
  - .agpr_count:     0
    .args:
      - .offset:         0
        .size:           256
        .value_kind:     by_value
      - .offset:         256
        .size:           4
        .value_kind:     hidden_block_count_x
      - .offset:         260
        .size:           4
        .value_kind:     hidden_block_count_y
      - .offset:         264
        .size:           4
        .value_kind:     hidden_block_count_z
      - .offset:         268
        .size:           2
        .value_kind:     hidden_group_size_x
      - .offset:         270
        .size:           2
        .value_kind:     hidden_group_size_y
      - .offset:         272
        .size:           2
        .value_kind:     hidden_group_size_z
      - .offset:         274
        .size:           2
        .value_kind:     hidden_remainder_x
      - .offset:         276
        .size:           2
        .value_kind:     hidden_remainder_y
      - .offset:         278
        .size:           2
        .value_kind:     hidden_remainder_z
      - .offset:         296
        .size:           8
        .value_kind:     hidden_global_offset_x
      - .offset:         304
        .size:           8
        .value_kind:     hidden_global_offset_y
      - .offset:         312
        .size:           8
        .value_kind:     hidden_global_offset_z
      - .offset:         320
        .size:           2
        .value_kind:     hidden_grid_dims
      - .offset:         376
        .size:           4
        .value_kind:     hidden_dynamic_lds_size
    .group_segment_fixed_size: 0
    .kernarg_segment_align: 8
    .kernarg_segment_size: 512
    .language:       OpenCL C
    .language_version:
      - 2
      - 0
    .max_flat_workgroup_size: 512
    .name:           _Z3fwd1P
    .private_segment_fixed_size: 0
    .sgpr_count:     107
    .sgpr_spill_count: 169
    .symbol:         _Z3fwd1P.kd
    .uniform_work_group_size: 1
    .uses_dynamic_stack: false
    .vgpr_count:     254
    .vgpr_spill_count: 0
    .wavefront_size: 64
  - .agpr_count:     0
    .args:
      - .offset:         0
        .size:           40
        .value_kind:     by_value
    .group_segment_fixed_size: 8704
    .kernarg_segment_align: 8
    .kernarg_segment_size: 40
    .language:       OpenCL C
    .language_version:
      - 2
      - 0
    .max_flat_workgroup_size: 256
    .name:           _Z5ngemmI3F1bEvT_
    .private_segment_fixed_size: 0
    .sgpr_count:     20
    .sgpr_spill_count: 0
    .symbol:         _Z5ngemmI3F1bEvT_.kd
    .uniform_work_group_size: 1
    .uses_dynamic_stack: false
    .vgpr_count:     68
    .vgpr_spill_count: 0
    .wavefront_size: 64
; __device__ __forceinline__ float fp8_to_f(unsigned b) { const unsigned s = (b >> 7) & 1u, e = (b >> 3) & 15u, m = b & 7u; const float v = e ? ldexpf(1.0f + (float)m * 0.125f, (int)e - 7) : ldexpf((float)m * 0.125f, -6); return s ? -v : v; }
;     __device__ bool valid(int bm) const { return (bm >> 2) < toff[NE]; }
;     __device__ bool valid(int bm) const { return (bm >> 2) < toff[NE]; }
; template <class F>
; __global__ void __launch_bounds__(256) ngemm(F f) {
;     __shared__ float As[16][68], Bs[16][68];
;     const int tx = threadIdx.x & 15, ty = threadIdx.x >> 4, bm = blockIdx.y, bn = blockIdx.x;
;     if (!f.valid(bm)) return;
;     const int lr = threadIdx.x >> 2, lk = (threadIdx.x & 3) * 4;
;     const unsigned char* ap = (const unsigned char*)f.aptr(bm * 64 + lr);
;     const unsigned char* bp = (const unsigned char*)f.bptr(bm, bn, lr);
;     float acc[4][4];
; #pragma unroll
;     for (int i = 0; i < 4; ++i)
; #pragma unroll
;         for (int j = 0; j < 4; ++j) acc[i][j] = 0.f;
;     for (int k0 = 0; k0 < F::K; k0 += 16) {
;         f.mid(k0, bm, ty, acc);
;         if constexpr (F::FP8) { const unsigned av = *(const unsigned*)(ap + k0 + lk), bv = *(const unsigned*)(bp + k0 + lk);
; #pragma unroll
;             for (int q = 0; q < 4; ++q) { As[lk + q][lr] = fp8_to_f((av >> (8 * q)) & 255u); Bs[lk + q][lr] = fp8_to_f((bv >> (8 * q)) & 255u) * W8_INV; } }
;         else { const v2u av = *(const v2u*)(ap + 2 * (k0 + lk)), bv = *(const v2u*)(bp + 2 * (k0 + lk));
;         As[lk + 0][lr] = __uint_as_float(av.x << 16); As[lk + 1][lr] = __uint_as_float(av.x & 0xffff0000u);
;         As[lk + 2][lr] = __uint_as_float(av.y << 16); As[lk + 3][lr] = __uint_as_float(av.y & 0xffff0000u);
;         Bs[lk + 0][lr] = __uint_as_float(bv.x << 16); Bs[lk + 1][lr] = __uint_as_float(bv.x & 0xffff0000u);
;         Bs[lk + 2][lr] = __uint_as_float(bv.y << 16); Bs[lk + 3][lr] = __uint_as_float(bv.y & 0xffff0000u); }
;         __syncthreads();
; #pragma unroll
;         for (int kk = 0; kk < 16; ++kk) {
;             const f32x4 a = *(const f32x4*)&As[kk][ty * 4], b = *(const f32x4*)&Bs[kk][tx * 4];
; #pragma unroll
;             for (int i = 0; i < 4; ++i)
; #pragma unroll
;                 for (int j = 0; j < 4; ++j) acc[i][j] += a[i] * b[j];
;         }
;         __syncthreads();
;     }
;     f.out(bm, bn, ty, tx, acc);
; }
  - .agpr_count:     0
    .args:
      - .offset:         0
        .size:           40
        .value_kind:     by_value
    .group_segment_fixed_size: 8704
    .kernarg_segment_align: 8
    .kernarg_segment_size: 40
    .language:       OpenCL C
    .language_version:
      - 2
      - 0
    .max_flat_workgroup_size: 256
    .name:           _Z5ngemmI2F1EvT_
    .private_segment_fixed_size: 0
    .sgpr_count:     20
    .sgpr_spill_count: 0
    .symbol:         _Z5ngemmI2F1EvT_.kd
    .uniform_work_group_size: 1
    .uses_dynamic_stack: false
    .vgpr_count:     66
    .vgpr_spill_count: 0
    .wavefront_size: 64
  - .agpr_count:     0
    .args:
      - .offset:         0
        .size:           56
        .value_kind:     by_value
    .group_segment_fixed_size: 8704
    .kernarg_segment_align: 8
    .kernarg_segment_size: 56
    .language:       OpenCL C
    .language_version:
      - 2
      - 0
    .max_flat_workgroup_size: 256
    .name:           _Z5ngemmI2F4EvT_
    .private_segment_fixed_size: 0
    .sgpr_count:     25
    .sgpr_spill_count: 0
    .symbol:         _Z5ngemmI2F4EvT_.kd
    .uniform_work_group_size: 1
    .uses_dynamic_stack: false
    .vgpr_count:     62
    .vgpr_spill_count: 0
    .wavefront_size: 64
  - .agpr_count:     0
    .args:
      - .offset:         0
        .size:           32
        .value_kind:     by_value
    .group_segment_fixed_size: 8704
    .kernarg_segment_align: 8
    .kernarg_segment_size: 32
    .language:       OpenCL C
    .language_version:
      - 2
      - 0
    .max_flat_workgroup_size: 256
    .name:           _Z5ngemmI2F5EvT_
    .private_segment_fixed_size: 0
    .sgpr_count:     18
    .sgpr_spill_count: 0
    .symbol:         _Z5ngemmI2F5EvT_.kd
    .uniform_work_group_size: 1
    .uses_dynamic_stack: false
    .vgpr_count:     102
    .vgpr_spill_count: 0
    .wavefront_size: 64
  - .agpr_count:     0
    .args:
      - .offset:         0
        .size:           32
        .value_kind:     by_value
    .group_segment_fixed_size: 8704
    .kernarg_segment_align: 8
    .kernarg_segment_size: 32
    .language:       OpenCL C
    .language_version:
      - 2
      - 0
    .max_flat_workgroup_size: 256
    .name:           _Z5ngemmI2F7EvT_
    .private_segment_fixed_size: 0
    .sgpr_count:     18
    .sgpr_spill_count: 0
    .symbol:         _Z5ngemmI2F7EvT_.kd
    .uniform_work_group_size: 1
    .uses_dynamic_stack: false
    .vgpr_count:     68
    .vgpr_spill_count: 0
    .wavefront_size: 64
  - .agpr_count:     0
    .args:
      - .offset:         0
        .size:           64
        .value_kind:     by_value
    .group_segment_fixed_size: 8704
    .kernarg_segment_align: 8
    .kernarg_segment_size: 64
    .language:       OpenCL C
    .language_version:
      - 2
      - 0
    .max_flat_workgroup_size: 256
    .name:           _Z5ngemmI2F9EvT_
    .private_segment_fixed_size: 0
    .sgpr_count:     40
    .sgpr_spill_count: 0
    .symbol:         _Z5ngemmI2F9EvT_.kd
    .uniform_work_group_size: 1
    .uses_dynamic_stack: false
    .vgpr_count:     68
    .vgpr_spill_count: 0
    .wavefront_size: 64
  - .agpr_count:     0
    .args:
      - .offset:         0
        .size:           40
        .value_kind:     by_value
    .group_segment_fixed_size: 8704
    .kernarg_segment_align: 8
    .kernarg_segment_size: 40
    .language:       OpenCL C
    .language_version:
      - 2
      - 0
    .max_flat_workgroup_size: 256
    .name:           _Z5ngemmI3F10EvT_
    .private_segment_fixed_size: 0
    .sgpr_count:     35
    .sgpr_spill_count: 0
    .symbol:         _Z5ngemmI3F10EvT_.kd
    .uniform_work_group_size: 1
    .uses_dynamic_stack: false
    .vgpr_count:     68
    .vgpr_spill_count: 0
    .wavefront_size: 64
